# v023 with 8 phase-2 late tiles per gMLP WG (7 W1 + 1 W2), dedicated converters 5984
# speedup vs baseline: 1.0048x; 1.0048x over previous
.LBB0_86:
	s_cmp_lt_i32 s50, 2
	s_cselect_b64 s[6:7], -1, 0
	s_and_b64 s[0:1], s[6:7], s[2:3]
	s_andn2_b64 vcc, exec, s[0:1]
	v_writelane_b32 v254, s60, 4
	s_cbranch_vccnz .LBB0_260
	s_mov_b64 s[2:3], s[80:81]
	s_load_dwordx2 s[8:9], s[2:3], 0xa8
	s_cmpk_lg_i32 s56, 0x100
	s_cselect_b32 s0, s56, 0xc8
	s_cmp_ge_i32 s78, s0
	s_mov_b64 s[4:5], -1
	s_cbranch_scc0 .LBB0_145
	s_sub_i32 s1, s78, s0
	s_cmpk_gt_i32 s1, 0x175f
	s_cbranch_scc1 .LBB0_144
	s_sub_i32 s20, s56, s0
	s_abs_i32 s4, s20
	v_cvt_f32_u32_e32 v1, s4
	s_load_dwordx2 s[10:11], s[2:3], 0x78
	s_load_dwordx2 s[12:13], s[2:3], 0x88
	s_sub_i32 s2, s20, s1
	s_add_i32 s3, s2, 0x175f
	v_rcp_iflag_f32_e32 v1, v1
	s_sub_i32 s2, 0xffffe8a1, s2
	s_xor_b32 s14, s3, s20
	s_sub_i32 s5, 0, s4
	v_mul_f32_e32 v1, 0x4f7ffffe, v1
	v_cvt_u32_f32_e32 v1, v1
	s_max_i32 s2, s3, s2
	s_ashr_i32 s3, s14, 31
	v_readfirstlane_b32 s14, v1
	s_mul_i32 s5, s5, s14
	s_mul_hi_u32 s5, s14, s5
	s_add_i32 s14, s14, s5
	s_mul_hi_u32 s5, s2, s14
	s_mul_i32 s14, s5, s4
	s_sub_i32 s2, s2, s14
	s_add_i32 s14, s5, 1
	s_sub_i32 s15, s2, s4
	s_cmp_ge_u32 s2, s4
	s_cselect_b32 s5, s14, s5
	s_cselect_b32 s2, s15, s2
	s_add_i32 s14, s5, 1
	s_cmp_ge_u32 s2, s4
	s_cselect_b32 s2, s14, s5
	s_xor_b32 s2, s2, s3
	s_sub_i32 s29, s2, s3
	s_lshl_b32 s21, s29, 2
	s_add_i32 s22, s21, -1
	s_cmp_gt_i32 s29, 0
	s_cselect_b64 s[2:3], -1, 0
	s_and_b64 s[4:5], s[2:3], exec
	s_cselect_b32 s18, 0, s22
	s_ashr_i32 s4, s18, 2
	s_mul_i32 s17, s4, s20
	s_add_i32 s17, s17, s1
	s_cmpk_gt_i32 s17, 0x1fff
	s_mov_b32 s5, 0
	s_cbranch_scc0 .LBB0_91
	s_add_i32 s4, s17, 0xffffe000
	s_lshr_b32 s4, s4, 7
	s_lshl_b64 s[4:5], s[4:5], 24
	s_waitcnt lgkmcnt(0)
	s_add_u32 s14, s12, s4
	s_addc_u32 s15, s13, s5
	s_lshl_b32 s4, s17, 4
	s_and_b32 s26, s4, 0x780
	s_lshl_b32 s4, s17, 8
	s_and_b32 s16, s4, 0x700
	s_mov_b64 s[4:5], 0x800
	s_cbranch_execz .LBB0_92
	s_branch .LBB0_93

.LBB0_160:
	s_add_i32 s89, s59, -1
	s_cmp_lt_u32 s89, 8
	s_cselect_b32 s88, 1, 0
	s_cbranch_scc0 .Lp1c_skip1
	s_and_b32 s90, s89, 1
	s_lshr_b32 s91, s57, 2
	s_cmp_eq_u32 s90, s91
	s_cselect_b32 s88, 1, 0
	s_cbranch_scc0 .Lp1c_skip1
	s_lshr_b32 s89, s89, 1
	s_mul_i32 s89, s89, 200
	s_add_u32 s89, s89, s78
	s_add_u32 s89, s89, 5984
	s_cmp_lt_u32 s89, 0x2000
	s_cselect_b32 s88, 1, 0
	s_cbranch_scc0 .Lp1c_skip1
	s_lshr_b32 s90, s89, 4
	s_lshl_b32 s90, s90, 21
	s_and_b32 s91, s89, 15
	s_lshl_b32 s92, s91, 10
	s_or_b32 s90, s90, s92
	s_lshl_b32 s92, s57, 7
	s_or_b32 s90, s90, s92
	s_add_u32 s84, s82, s90
	s_addc_u32 s85, s83, 0
	s_lshr_b32 s90, s89, 8
	s_lshl_b32 s90, s90, 23
	s_lshl_b32 s91, s91, 19
	s_or_b32 s90, s90, s91
	s_bfe_u32 s91, s89, 0x40004
	s_lshl_b32 s91, s91, 7
	s_or_b32 s90, s90, s91
	s_lshl_b32 s91, s57, 15
	s_or_b32 s90, s90, s91
	s_add_u32 s90, s90, 0x4ee00000
	s_add_u32 s86, s48, s90
	s_addc_u32 s87, s49, 0
	global_load_dwordx4 v[180:183], v245, s[84:85] nt
	s_add_u32 s84, s84, 0x4000
	s_addc_u32 s85, s85, 0
	global_load_dwordx4 v[184:187], v245, s[84:85] nt
	s_add_u32 s84, s84, 0x4000
	s_addc_u32 s85, s85, 0
	global_load_dwordx4 v[188:191], v245, s[84:85] nt
	s_add_u32 s84, s84, 0x4000
	s_addc_u32 s85, s85, 0
	global_load_dwordx4 v[192:195], v245, s[84:85] nt
	s_add_u32 s84, s84, 0x4000
	s_addc_u32 s85, s85, 0
	global_load_dwordx4 v[196:199], v245, s[84:85] nt
	s_add_u32 s84, s84, 0x4000
	s_addc_u32 s85, s85, 0
	global_load_dwordx4 v[200:203], v245, s[84:85] nt
	s_add_u32 s84, s84, 0x4000
	s_addc_u32 s85, s85, 0
	global_load_dwordx4 v[204:207], v245, s[84:85] nt
	s_add_u32 s84, s84, 0x4000
	s_addc_u32 s85, s85, 0
	global_load_dwordx4 v[208:211], v245, s[84:85] nt
	s_add_u32 s84, s84, 0x4000
	s_addc_u32 s85, s85, 0
	global_load_dwordx4 v[212:215], v245, s[84:85] nt
	s_add_u32 s84, s84, 0x4000
	s_addc_u32 s85, s85, 0
	global_load_dwordx4 v[216:219], v245, s[84:85] nt
	s_add_u32 s84, s84, 0x4000
	s_addc_u32 s85, s85, 0
	global_load_dwordx4 v[220:223], v245, s[84:85] nt
	s_add_u32 s84, s84, 0x4000
	s_addc_u32 s85, s85, 0
	global_load_dwordx4 v[224:227], v245, s[84:85] nt
	s_add_u32 s84, s84, 0x4000
	s_addc_u32 s85, s85, 0
	global_load_dwordx4 v[228:231], v245, s[84:85] nt
	s_add_u32 s84, s84, 0x4000
	s_addc_u32 s85, s85, 0
	global_load_dwordx4 v[232:235], v245, s[84:85] nt
	s_add_u32 s84, s84, 0x4000
	s_addc_u32 s85, s85, 0
	global_load_dwordx4 v[236:239], v245, s[84:85] nt
	s_add_u32 s84, s84, 0x4000
	s_addc_u32 s85, s85, 0
	global_load_dwordx4 v[240:243], v245, s[84:85] nt

.LBB0_367:
	s_lshr_b32 s0, s56, 31
	s_add_i32 s0, s56, s0
	s_ashr_i32 s0, s0, 1
	v_readlane_b32 s78, v254, 5
	s_cmp_ge_i32 s78, s0
	v_readlane_b32 s79, v254, 8
	v_readlane_b32 s60, v254, 4
	s_cbranch_scc0 .LBB0_409
	s_sub_i32 s10, s78, s0
	s_cmpk_gt_u32 s10, 0x37f
	s_waitcnt vmcnt(0) lgkmcnt(0)
	s_barrier
	s_cbranch_scc1 .LBB0_409
	s_sub_i32 s0, s56, s0
	s_abs_i32 s2, s0
	v_cvt_f32_u32_e32 v2, s2
	s_sub_i32 s3, s0, s10
	s_add_i32 s4, s3, 0x37f
	s_sub_i32 s3, 0xfffffc81, s3
	v_rcp_iflag_f32_e32 v2, v2
	s_xor_b32 s6, s4, s0
	s_sub_i32 s5, 0, s2
	s_max_i32 s3, s4, s3
	v_mul_f32_e32 v2, 0x4f7ffffe, v2
	v_cvt_u32_f32_e32 v2, v2
	s_ashr_i32 s4, s6, 31
	s_add_i32 s1, s10, 0x2000
	v_readfirstlane_b32 s6, v2
	s_mul_i32 s5, s5, s6
	s_mul_hi_u32 s5, s6, s5
	s_add_i32 s6, s6, s5
	s_mul_hi_u32 s5, s3, s6
	s_mul_i32 s6, s5, s2
	s_sub_i32 s3, s3, s6
	s_add_i32 s7, s5, 1
	s_sub_i32 s6, s3, s2
	s_cmp_ge_u32 s3, s2
	s_cselect_b32 s5, s7, s5
	s_cselect_b32 s3, s6, s3
	s_add_i32 s6, s5, 1
	s_cmp_ge_u32 s3, s2
	s_cselect_b32 s2, s6, s5
	s_xor_b32 s2, s2, s4
	s_sub_i32 s18, s2, s4
	s_mov_b32 s18, 8
	s_movk_i32 s0, 0xff80
	s_lshl_b32 s12, s18, 2
	s_add_i32 s13, s12, -1
	s_cmp_gt_i32 s18, 0
	s_cselect_b64 s[2:3], -1, 0
	s_and_b64 s[4:5], s[2:3], exec
	s_cselect_b32 s11, 0, s13
	s_ashr_i32 s4, s11, 2
	s_mul_i32 s9, s4, s0
	s_add_i32 s9, s9, s1
	s_cmpk_gt_i32 s9, 0x1fff
	s_mov_b32 s5, 0
	s_cbranch_scc0 .LBB0_371
	s_add_i32 s4, s9, 0xffffe000
	s_lshr_b32 s4, s4, 7
	s_lshl_b64 s[4:5], s[4:5], 24
	v_readlane_b32 s34, v254, 13
	v_readlane_b32 s35, v254, 14
	s_add_u32 s6, s34, s4
	s_addc_u32 s7, s35, s5
	s_lshl_b32 s4, s9, 4
	s_and_b32 s19, s4, 0x780
	s_lshl_b32 s4, s9, 8
	v_readlane_b32 s30, v254, 11
	s_and_b32 s8, s4, 0x700
	v_readlane_b32 s31, v254, 12
	s_mov_b64 s[4:5], 0x800
	s_cbranch_execz .LBB0_372
	s_branch .LBB0_373

.LBB0_537:
	s_add_i32 s89, s58, -1
	s_cmp_lt_u32 s89, 2
	s_cselect_b32 s88, 1, 0
	s_cbranch_scc0 .Lp4c_skip1
	s_mul_i32 s89, s89, 256
	s_add_u32 s89, s89, s78
	s_add_u32 s89, s89, 6784
	s_cmp_lt_u32 s89, 0x2000
	s_cselect_b32 s88, 1, 0
	s_cbranch_scc0 .Lp4c_skip1
	s_lshr_b32 s90, s89, 4
	s_lshl_b32 s90, s90, 21
	s_and_b32 s91, s89, 15
	s_lshl_b32 s92, s91, 10
	s_or_b32 s90, s90, s92
	s_lshl_b32 s92, s57, 7
	s_or_b32 s90, s90, s92
	s_add_u32 s84, s82, s90
	s_addc_u32 s85, s83, 0
	s_lshr_b32 s90, s89, 8
	s_lshl_b32 s90, s90, 23
	s_lshl_b32 s91, s91, 19
	s_or_b32 s90, s90, s91
	s_bfe_u32 s91, s89, 0x40004
	s_lshl_b32 s91, s91, 7
	s_or_b32 s90, s90, s91
	s_lshl_b32 s91, s57, 15
	s_or_b32 s90, s90, s91
	s_add_u32 s90, s90, 0x4ee00000
	s_add_u32 s86, s48, s90
	s_addc_u32 s87, s49, 0
	global_load_dwordx4 v[180:183], v245, s[84:85] nt
	s_add_u32 s84, s84, 0x4000
	s_addc_u32 s85, s85, 0
	global_load_dwordx4 v[184:187], v245, s[84:85] nt
	s_add_u32 s84, s84, 0x4000
	s_addc_u32 s85, s85, 0
	global_load_dwordx4 v[188:191], v245, s[84:85] nt
	s_add_u32 s84, s84, 0x4000
	s_addc_u32 s85, s85, 0
	global_load_dwordx4 v[192:195], v245, s[84:85] nt
	s_add_u32 s84, s84, 0x4000
	s_addc_u32 s85, s85, 0
	global_load_dwordx4 v[196:199], v245, s[84:85] nt
	s_add_u32 s84, s84, 0x4000
	s_addc_u32 s85, s85, 0
	global_load_dwordx4 v[200:203], v245, s[84:85] nt
	s_add_u32 s84, s84, 0x4000
	s_addc_u32 s85, s85, 0
	global_load_dwordx4 v[204:207], v245, s[84:85] nt
	s_add_u32 s84, s84, 0x4000
	s_addc_u32 s85, s85, 0
	global_load_dwordx4 v[208:211], v245, s[84:85] nt
	s_add_u32 s84, s84, 0x4000
	s_addc_u32 s85, s85, 0
	global_load_dwordx4 v[212:215], v245, s[84:85] nt
	s_add_u32 s84, s84, 0x4000
	s_addc_u32 s85, s85, 0
	global_load_dwordx4 v[216:219], v245, s[84:85] nt
	s_add_u32 s84, s84, 0x4000
	s_addc_u32 s85, s85, 0
	global_load_dwordx4 v[220:223], v245, s[84:85] nt
	s_add_u32 s84, s84, 0x4000
	s_addc_u32 s85, s85, 0
	global_load_dwordx4 v[224:227], v245, s[84:85] nt
	s_add_u32 s84, s84, 0x4000
	s_addc_u32 s85, s85, 0
	global_load_dwordx4 v[228:231], v245, s[84:85] nt
	s_add_u32 s84, s84, 0x4000
	s_addc_u32 s85, s85, 0
	global_load_dwordx4 v[232:235], v245, s[84:85] nt
	s_add_u32 s84, s84, 0x4000
	s_addc_u32 s85, s85, 0
	global_load_dwordx4 v[236:239], v245, s[84:85] nt
	s_add_u32 s84, s84, 0x4000
	s_addc_u32 s85, s85, 0
	global_load_dwordx4 v[240:243], v245, s[84:85] nt
